# GDN chunk unit S1: gate-log prefix sum in registers (DPP row_shr + row_bcast) instead of six ds_bpermute round trips; on top of the fetch2 running pointers
# speedup vs baseline: 1.0182x; 1.0052x over previous
; #define LAS __attribute__((address_space(3)))
; __device__ __forceinline__ unsigned f2bf(float f) { unsigned u = __float_as_uint(f); return (u + 0x7fffu + ((u >> 16) & 1u)) >> 16; }
; __device__ __forceinline__ float rdlane_f(float v, int l) { return __builtin_bit_cast(float, __builtin_amdgcn_readlane(__builtin_bit_cast(int, v), l)); }
; __device__ __forceinline__ float gdn_s1(const GdnIn& in, LAS unsigned char* ub, LAS unsigned char* dwb, int w, int lane) {
;     ...
;     float beta = in.g2.x, cum = in.g2.y;
; #pragma unroll
;     for (int o = 1; o < 64; o <<= 1) { const float t = __shfl_up(cum, o); if (lane >= o) cum += t; }
;     const float cl = rdlane_f(cum, 63);
;     GT[lane] = beta; GT[64 + lane] = cum; GT[128 + lane] = __expf(cum);
;     asm volatile("s_waitcnt lgkmcnt(0)" ::: "memory");
;     { const f32x4 ci = *(const LAS f32x4*)(GT + 64 + 16 * I1 + 4 * kg), bi = *(const LAS f32x4*)(GT + 16 * I1 + 4 * kg);
; #pragma unroll
;       for (int jj = 0; jj < 2; ++jj) { const int J = 2 * (w & 1) + jj;
;           f32x4 ck = (f32x4){0.f, 0.f, 0.f, 0.f}, cq = (f32x4){0.f, 0.f, 0.f, 0.f};
; #pragma unroll
;           for (int s = 0; s < 2; ++s) { ck = __builtin_amdgcn_mfma_f32_16x16x32_bf16(in.ak[s], in.bk[jj][s], ck, 0, 0, 0); cq = __builtin_amdgcn_mfma_f32_16x16x32_bf16(in.aq[s], in.bk[jj][s], cq, 0, 0, 0); }
;           const int j = 16 * J + fr; const float cj = GT[64 + j];
; #pragma unroll
;           for (int e = 0; e < 4; ++e) { const int i = 16 * I1 + 4 * kg + e; const float gm = __expf(fminf(ci[e] - cj, 0.f));
;               AB[i * 72 + j] = (bf16)f2bf(j < i ? bi[e] * ck[e] * gm : 0.f); ATT[i * 72 + j] = (bf16)f2bf(j <= i ? cq[e] * gm : 0.f); } } }
.Lgf2a_done:
.LBB0_1719:
	v_mov_b32_e32 v66, v113
	v_add_u32_e32 v67, s42, v54
	s_nop 1
	v_add_f32_dpp v66, v66, v66 row_shr:1 row_mask:0xf bank_mask:0xf
	v_mfma_f32_16x16x32_bf16 v[58:61], v[6:9], v[10:13], 0
	s_nop 1
	v_add_f32_dpp v66, v66, v66 row_shr:2 row_mask:0xf bank_mask:0xf
	s_movk_i32 s2, 0x48
	s_nop 1
	v_add_f32_dpp v66, v66, v66 row_shr:4 row_mask:0xf bank_mask:0xf
	v_or_b32_e32 v69, 1, v67
	s_nop 1
	v_add_f32_dpp v66, v66, v66 row_shr:8 row_mask:0xf bank_mask:0xf
	v_or_b32_e32 v70, 2, v67
	s_nop 1
	v_add_f32_dpp v66, v66, v66 row_bcast:15 row_mask:0xa bank_mask:0xf
	s_add_i32 s28, s26, 1
	s_nop 1
	v_add_f32_dpp v66, v66, v66 row_bcast:31 row_mask:0xc bank_mask:0xf
	s_mov_b64 s[48:49], -1
	v_mul_f32_e32 v33, 0x3fb8aa3b, v66
	v_exp_f32_e32 v33, v33
	v_lshl_add_u32 v32, v110, 2, s8
	ds_write2st64_b32 v32, v112, v66 offset0:224 offset1:225
	v_readlane_b32 s36, v66, 63
	ds_write_b32 v32, v33 offset:57856
	s_waitcnt lgkmcnt(0)
	v_lshl_add_u32 v32, v54, 2, s30
	v_mfma_f32_16x16x32_bf16 v[54:57], v[2:5], v[10:13], 0
	ds_read_b128 v[50:53], v32 offset:57600
	ds_read_b128 v[46:49], v32 offset:57344
	v_or_b32_e32 v32, s43, v119
	v_lshl_add_u32 v33, v32, 2, s8
	v_add_u32_e32 v33, 0xe000, v33
	v_mfma_f32_16x16x32_bf16 v[62:65], v[18:21], v[26:29], v[54:57]
	v_cmp_lt_i32_e32 vcc, v32, v67
	s_nop 1
	ds_read2_b32 v[54:55], v33 offset0:64 offset1:80
	v_mfma_f32_16x16x32_bf16 v[56:59], v[22:25], v[26:29], v[58:61]
	s_waitcnt lgkmcnt(0)
	v_sub_f32_e32 v33, v50, v54
	v_min_f32_e32 v33, 0, v33
	v_mul_f32_e32 v33, 0x3fb8aa3b, v33
	v_exp_f32_e32 v33, v33
	v_mul_f32_e32 v60, v46, v62
	v_sub_f32_e32 v50, v50, v55
	v_min_f32_e32 v50, 0, v50
	v_mul_f32_e32 v60, v60, v33
	v_cndmask_b32_e32 v60, 0, v60, vcc
	v_bfe_u32 v61, v60, 16, 1
	v_add3_u32 v62, v60, v61, s81
	v_mad_u64_u32 v[60:61], s[2:3], v67, s2, v[32:33]
	v_cmp_gt_i32_e32 vcc, v32, v67
	v_mul_f32_e32 v33, v56, v33
	v_lshl_add_u32 v68, v60, 1, 0
	v_cndmask_b32_e64 v33, v33, 0, vcc
	v_cvt_pk_bf16_f32 v33, v33, v33
	ds_write_b16 v68, v33 offset:9216
	v_sub_f32_e32 v33, v51, v54
	v_min_f32_e32 v33, 0, v33
	v_mul_f32_e32 v33, 0x3fb8aa3b, v33
	v_exp_f32_e32 v33, v33
	v_mul_f32_e32 v56, v47, v63
	v_mul_f32_e32 v50, 0x3fb8aa3b, v50
	ds_write_b16_d16_hi v68, v62
	v_mul_f32_e32 v56, v56, v33
	v_cndmask_b32_e64 v56, v56, 0, vcc
	v_bfe_u32 v60, v56, 16, 1
	v_mul_f32_e32 v33, v57, v33
	v_cmp_le_i32_e32 vcc, v32, v69
	v_add3_u32 v56, v56, v60, s81
	ds_write_b16_d16_hi v68, v56 offset:144
	v_cndmask_b32_e32 v33, 0, v33, vcc
	v_cvt_pk_bf16_f32 v33, v33, v33
	ds_write_b16 v68, v33 offset:9360
	v_sub_f32_e32 v33, v52, v54
	v_min_f32_e32 v33, 0, v33
	v_mul_f32_e32 v33, 0x3fb8aa3b, v33
	v_exp_f32_e32 v33, v33
	v_mul_f32_e32 v56, v48, v64
	v_cmp_lt_i32_e32 vcc, v32, v70
	v_or_b32_e32 v64, 3, v67
	v_mul_f32_e32 v56, v56, v33
	v_cndmask_b32_e32 v56, 0, v56, vcc
	v_bfe_u32 v57, v56, 16, 1
	v_mul_f32_e32 v33, v58, v33
	v_cmp_le_i32_e32 vcc, v32, v70
	v_add3_u32 v56, v56, v57, s81
	ds_write_b16_d16_hi v68, v56 offset:288
	v_cndmask_b32_e32 v33, 0, v33, vcc
	v_cvt_pk_bf16_f32 v33, v33, v33
	ds_write_b16 v68, v33 offset:9504
	v_sub_f32_e32 v33, v53, v54
	v_min_f32_e32 v33, 0, v33
	v_mul_f32_e32 v33, 0x3fb8aa3b, v33
	v_exp_f32_e32 v33, v33
	v_mul_f32_e32 v54, v49, v65
	v_cmp_lt_i32_e32 vcc, v32, v64
	v_mfma_f32_16x16x32_bf16 v[60:63], v[6:9], v[14:17], 0
	v_mul_f32_e32 v54, v54, v33
	v_cndmask_b32_e32 v54, 0, v54, vcc
	v_bfe_u32 v56, v54, 16, 1
	v_add3_u32 v54, v54, v56, s81
	v_mul_f32_e32 v33, v59, v33
	v_mfma_f32_16x16x32_bf16 v[56:59], v[2:5], v[14:17], 0
	v_cmp_le_i32_e32 vcc, v32, v64
	v_exp_f32_e32 v50, v50
	ds_write_b16_d16_hi v68, v54 offset:432
	v_mfma_f32_16x16x32_bf16 v[56:59], v[18:21], v[36:39], v[56:59]
	v_cndmask_b32_e32 v33, 0, v33, vcc
	v_cvt_pk_bf16_f32 v33, v33, v33
	ds_write_b16 v68, v33 offset:9648
	v_or_b32_e32 v33, 16, v32
	s_nop 2
	s_nop 0
	v_mul_f32_e32 v46, v46, v56
	v_mfma_f32_16x16x32_bf16 v[60:63], v[22:25], v[36:39], v[60:63]
	v_cmp_lt_i32_e32 vcc, v33, v67
	v_mul_f32_e32 v46, v46, v50
	v_mul_f32_e32 v47, v47, v57
	v_cndmask_b32_e32 v46, 0, v46, vcc
	v_cvt_pk_bf16_f32 v46, v46, v46
	ds_write_b16 v68, v46 offset:32
	v_cmp_gt_i32_e32 vcc, v33, v67
	s_nop 0
	v_mul_f32_e32 v46, v60, v50
	v_mul_lo_u32 v54, v110, s75
	v_cndmask_b32_e64 v46, v46, 0, vcc
	v_cvt_pk_bf16_f32 v46, v46, v46
	ds_write_b16 v68, v46 offset:9248
	v_sub_f32_e32 v46, v51, v55
	v_min_f32_e32 v46, 0, v46
	v_mul_f32_e32 v46, 0x3fb8aa3b, v46
	v_exp_f32_e32 v46, v46
	v_lshlrev_b32_e32 v57, 16, v1
	v_lshlrev_b32_e32 v56, 16, v30
	s_mov_b32 s2, 0x7060302
	v_mul_f32_e32 v47, v47, v46
	v_cndmask_b32_e64 v47, v47, 0, vcc
	v_mul_f32_e32 v46, v61, v46
	v_cmp_le_i32_e32 vcc, v33, v69
	v_cvt_pk_bf16_f32 v47, v47, v47
	ds_write_b16 v68, v47 offset:176
	v_cndmask_b32_e32 v46, 0, v46, vcc
	v_cvt_pk_bf16_f32 v46, v46, v46
	ds_write_b16 v68, v46 offset:9392
	v_sub_f32_e32 v46, v52, v55
	v_min_f32_e32 v46, 0, v46
	v_mul_f32_e32 v46, 0x3fb8aa3b, v46
	v_exp_f32_e32 v46, v46
	v_mul_f32_e32 v47, v48, v58
	v_cmp_lt_i32_e32 vcc, v33, v70
	v_mov_b32_e32 v50, s84
	v_mul_f32_e32 v47, v47, v46
	v_cndmask_b32_e32 v47, 0, v47, vcc
	v_mul_f32_e32 v46, v62, v46
	v_cmp_le_i32_e32 vcc, v33, v70
	v_cvt_pk_bf16_f32 v47, v47, v47
	ds_write_b16 v68, v47 offset:320
	v_cndmask_b32_e32 v46, 0, v46, vcc
	v_cvt_pk_bf16_f32 v46, v46, v46
	ds_write_b16 v68, v46 offset:9536
	v_sub_f32_e32 v46, v53, v55
	v_min_f32_e32 v46, 0, v46
	v_mul_f32_e32 v46, 0x3fb8aa3b, v46
	v_exp_f32_e32 v46, v46
	v_mul_f32_e32 v47, v49, v59
	v_cmp_lt_i32_e32 vcc, v33, v64
	v_add_u32_e32 v58, s11, v54
	v_mul_f32_e32 v47, v47, v46
	v_cndmask_b32_e32 v47, 0, v47, vcc
	v_mul_f32_e32 v46, v63, v46
	v_cmp_le_i32_e32 vcc, v33, v64
	v_cvt_pk_bf16_f32 v47, v47, v47
	ds_write_b16 v68, v47 offset:464
	v_cndmask_b32_e32 v46, 0, v46, vcc
	v_cvt_pk_bf16_f32 v46, v46, v46
	ds_write_b16 v68, v46 offset:9680
	ds_read_b128 v[46:49], v50 offset:57600
	ds_read_b128 v[50:53], v50 offset:57616
	v_lshlrev_b32_e32 v55, 16, v31
	v_lshlrev_b32_e32 v54, 16, v40
	s_waitcnt lgkmcnt(1)
; #define LAS __attribute__((address_space(3)))
; __device__ __forceinline__ unsigned f2bf(float f) { unsigned u = __float_as_uint(f); return (u + 0x7fffu + ((u >> 16) & 1u)) >> 16; }
; __device__ __forceinline__ float gdn_s1(const GdnIn& in, LAS unsigned char* ub, LAS unsigned char* dwb, int w, int lane) {
;     ...
;     { const f32x4 c8a = *(const LAS f32x4*)(GT + 64 + 8 * w), c8b = *(const LAS f32x4*)(GT + 64 + 8 * w + 4);
; #pragma unroll
;       for (int tt = 0; tt < 8; ++tt) KTT[lane * 72 + 8 * w + tt] = (bf16)f2bf(__uint_as_float(in.kt8[tt] << 16) * __expf(cl - (tt < 4 ? c8a[tt & 3] : c8b[tt & 3]))); }
;     asm volatile("s_waitcnt lgkmcnt(0)" ::: "memory");
;     return cl;
; __device__ __forceinline__ void gdn_chain_units(CArgs& a, int chain, LAS unsigned char* lds, int w, int lane, unsigned long long& tacc) {
;     ...
;           gdn_fetch2(a, chain * 36 + n, w, lane, C); const float cl = gdn_s1(A, lds, dwb, w, lane);
;           if (PROBE_PH == 60) tacc += __builtin_amdgcn_s_memrealtime() - tq; if (PROBE_PH == 61) tq = __builtin_amdgcn_s_memrealtime();
;           __syncthreads();
;           if (PROBE_PH == 61) tacc += __builtin_amdgcn_s_memrealtime() - tq; if (PROBE_PH >= 62 && PROBE_PH <= 64) tq = __builtin_amdgcn_s_memrealtime();
;           gdn_fetch(a, chain * 36 + n + 1, w, lane, B); gdn_s23(a, chain * 36 + n, C, lds, dwb, w, lane, cl);
	v_sub_f32_e32 v46, s36, v46
	v_sub_f32_e32 v47, s36, v47
	v_sub_f32_e32 v48, s36, v48
	v_sub_f32_e32 v49, s36, v49
	v_mul_f32_e32 v46, 0x3fb8aa3b, v46
	v_mul_f32_e32 v47, 0x3fb8aa3b, v47
	v_mul_f32_e32 v48, 0x3fb8aa3b, v48
	v_mul_f32_e32 v49, 0x3fb8aa3b, v49
	v_exp_f32_e32 v46, v46
	v_exp_f32_e32 v47, v47
	v_exp_f32_e32 v48, v48
	v_exp_f32_e32 v49, v49
	s_waitcnt lgkmcnt(0)
	v_sub_f32_e32 v50, s36, v50
	v_sub_f32_e32 v51, s36, v51
	v_sub_f32_e32 v52, s36, v52
	v_sub_f32_e32 v53, s36, v53
	v_mul_f32_e32 v50, 0x3fb8aa3b, v50
	v_mul_f32_e32 v51, 0x3fb8aa3b, v51
	v_mul_f32_e32 v52, 0x3fb8aa3b, v52
	v_mul_f32_e32 v53, 0x3fb8aa3b, v53
	v_exp_f32_e32 v50, v50
	v_exp_f32_e32 v51, v51
	v_exp_f32_e32 v52, v52
	v_exp_f32_e32 v53, v53
	v_pk_mul_f32 v[46:47], v[46:47], v[56:57]
	v_pk_mul_f32 v[48:49], v[48:49], v[54:55]
	v_bfe_u32 v56, v47, 16, 1
	v_bfe_u32 v54, v49, 16, 1
	v_bfe_u32 v55, v48, 16, 1
	v_bfe_u32 v57, v46, 16, 1
	v_add3_u32 v57, v46, v57, s81
	v_add3_u32 v56, v47, v56, s81
	v_add3_u32 v55, v48, v55, s81
	v_add3_u32 v54, v49, v54, s81
	v_lshlrev_b32_e32 v47, 16, v43
	v_lshlrev_b32_e32 v46, 16, v44
	v_lshlrev_b32_e32 v49, 16, v41
	v_lshlrev_b32_e32 v48, 16, v42
	v_pk_mul_f32 v[48:49], v[50:51], v[48:49]
	v_pk_mul_f32 v[46:47], v[52:53], v[46:47]
	v_bfe_u32 v52, v49, 16, 1
	v_bfe_u32 v50, v47, 16, 1
	v_bfe_u32 v51, v46, 16, 1
	v_bfe_u32 v53, v48, 16, 1
	v_add3_u32 v48, v48, v53, s81
	v_add3_u32 v52, v49, v52, s81
	v_add3_u32 v46, v46, v51, s81
	v_add3_u32 v47, v47, v50, s81
	v_perm_b32 v49, v47, v46, s2
	v_perm_b32 v48, v52, v48, s2
	v_perm_b32 v47, v54, v55, s2
	v_perm_b32 v46, v56, v57, s2
	s_mul_hi_i32 s2, s28, 0x38e38e39
	s_lshr_b32 s3, s2, 31
	s_ashr_i32 s9, s2, 3
	s_add_i32 s9, s9, s3
	s_mul_i32 s2, s9, 36
	s_sub_i32 s2, s28, s2
	ds_write_b128 v58, v[46:49] offset:18432
	s_ashr_i32 s29, s9, 3
	s_and_b32 s27, s9, 1
	s_lshl_b32 s20, s2, 6
	s_waitcnt lgkmcnt(0)
	s_cmp_gt_i32 s2, 3
	s_cselect_b64 s[56:57], -1, 0
	s_and_b64 vcc, exec, s[56:57]
	s_waitcnt lgkmcnt(0)
	s_barrier
	s_waitcnt vmcnt(0)
	v_lshlrev_b32_e32 v151, 16, v151
	v_lshlrev_b32_e32 v150, 16, v150
	v_lshlrev_b32_e32 v153, 16, v153
	v_lshlrev_b32_e32 v152, 16, v152
	v_lshlrev_b32_e32 v147, 16, v147
	v_lshlrev_b32_e32 v146, 16, v146
	v_lshlrev_b32_e32 v149, 16, v149
	v_lshlrev_b32_e32 v148, 16, v148
	v_lshlrev_b32_e32 v144, 16, v144
	v_lshlrev_b32_e32 v142, 16, v142
	v_lshlrev_b32_e32 v145, 16, v145
	v_lshlrev_b32_e32 v143, 16, v143
	v_lshlrev_b32_e32 v140, 16, v140
	v_lshlrev_b32_e32 v138, 16, v138
	v_lshlrev_b32_e32 v141, 16, v141
	v_lshlrev_b32_e32 v139, 16, v139
	s_cbranch_vccz .LBB0_1721
	s_add_i32 s2, s20, 0xffffff00
	s_lshl_b32 s3, s29, 11
	s_sub_i32 s48, 0x8ff, s20
	s_cmp_eq_u32 s27, 0
	s_cselect_b32 s2, s2, s48
	s_add_i32 s2, s3, s2
	s_addk_i32 s2, 0x1000
	s_mov_b64 s[48:49], 0

; #define LAS __attribute__((address_space(3)))
; __device__ __forceinline__ unsigned f2bf(float f) { unsigned u = __float_as_uint(f); return (u + 0x7fffu + ((u >> 16) & 1u)) >> 16; }
; __device__ __forceinline__ float rdlane_f(float v, int l) { return __builtin_bit_cast(float, __builtin_amdgcn_readlane(__builtin_bit_cast(int, v), l)); }
; __device__ __forceinline__ float gdn_s1(const GdnIn& in, LAS unsigned char* ub, LAS unsigned char* dwb, int w, int lane) {
;     ...
;     float beta = in.g2.x, cum = in.g2.y;
; #pragma unroll
;     for (int o = 1; o < 64; o <<= 1) { const float t = __shfl_up(cum, o); if (lane >= o) cum += t; }
;     const float cl = rdlane_f(cum, 63);
;     GT[lane] = beta; GT[64 + lane] = cum; GT[128 + lane] = __expf(cum);
;     asm volatile("s_waitcnt lgkmcnt(0)" ::: "memory");
;     { const f32x4 ci = *(const LAS f32x4*)(GT + 64 + 16 * I1 + 4 * kg), bi = *(const LAS f32x4*)(GT + 16 * I1 + 4 * kg);
; #pragma unroll
;       for (int jj = 0; jj < 2; ++jj) { const int J = 2 * (w & 1) + jj;
;           f32x4 ck = (f32x4){0.f, 0.f, 0.f, 0.f}, cq = (f32x4){0.f, 0.f, 0.f, 0.f};
; #pragma unroll
;           for (int s = 0; s < 2; ++s) { ck = __builtin_amdgcn_mfma_f32_16x16x32_bf16(in.ak[s], in.bk[jj][s], ck, 0, 0, 0); cq = __builtin_amdgcn_mfma_f32_16x16x32_bf16(in.aq[s], in.bk[jj][s], cq, 0, 0, 0); }
;           const int j = 16 * J + fr; const float cj = GT[64 + j];
; #pragma unroll
;           for (int e = 0; e < 4; ++e) { const int i = 16 * I1 + 4 * kg + e; const float gm = __expf(fminf(ci[e] - cj, 0.f));
;               AB[i * 72 + j] = (bf16)f2bf(j < i ? bi[e] * ck[e] * gm : 0.f); ATT[i * 72 + j] = (bf16)f2bf(j <= i ? cq[e] * gm : 0.f); } } }
.Lgf2b_done:
.LBB0_1775:
	s_waitcnt vmcnt(32)
	v_mov_b32_e32 v33, v115
	s_waitcnt vmcnt(29)
	v_mfma_f32_16x16x32_bf16 v[86:89], v[58:61], v[70:73], 0
	s_movk_i32 s2, 0x48
	v_add_f32_dpp v33, v33, v33 row_shr:1 row_mask:0xf bank_mask:0xf
	s_cmp_gt_u32 s0, 33
	v_mfma_f32_16x16x32_bf16 v[70:73], v[46:49], v[70:73], 0
	v_add_f32_dpp v33, v33, v33 row_shr:2 row_mask:0xf bank_mask:0xf
	s_cselect_b64 s[50:51], -1, 0
	s_nop 1
	v_add_f32_dpp v33, v33, v33 row_shr:4 row_mask:0xf bank_mask:0xf
	s_mov_b64 s[62:63], 0x40000
	s_waitcnt vmcnt(25)
	v_add_f32_dpp v33, v33, v33 row_shr:8 row_mask:0xf bank_mask:0xf
	v_mfma_f32_16x16x32_bf16 v[86:89], v[50:53], v[74:77], v[86:89]
	s_nop 1
	v_add_f32_dpp v33, v33, v33 row_bcast:15 row_mask:0xa bank_mask:0xf
	v_mfma_f32_16x16x32_bf16 v[70:73], v[54:57], v[74:77], v[70:73]
	v_mfma_f32_16x16x32_bf16 v[46:49], v[46:49], v[62:65], 0
	v_add_f32_dpp v33, v33, v33 row_bcast:31 row_mask:0xc bank_mask:0xf
	v_mfma_f32_16x16x32_bf16 v[58:61], v[58:61], v[62:65], 0
	v_mul_f32_e32 v78, 0x3fb8aa3b, v33
	v_exp_f32_e32 v78, v78
	v_lshl_add_u32 v32, v110, 2, s8
	ds_write2st64_b32 v32, v114, v33 offset0:224 offset1:225
	v_add_u32_e32 v114, s42, v34
	ds_write_b32 v32, v78 offset:57856
	s_waitcnt lgkmcnt(0)
	v_lshl_add_u32 v32, v34, 2, s30
	ds_read_b128 v[82:85], v32 offset:57600
	ds_read_b128 v[78:81], v32 offset:57344
	v_or_b32_e32 v32, s43, v106
	v_lshl_add_u32 v34, v32, 2, s8
	v_add_u32_e32 v34, 0xe000, v34
	ds_read2_b32 v[74:75], v34 offset0:64 offset1:80
	s_waitcnt lgkmcnt(1)
	v_mul_f32_e32 v76, v78, v86
	v_cmp_lt_i32_e32 vcc, v32, v114
	s_waitcnt vmcnt(24)
	v_mfma_f32_16x16x32_bf16 v[46:49], v[54:57], v[66:69], v[46:49]
	v_readlane_b32 s9, v33, 63
	s_waitcnt lgkmcnt(0)
	v_sub_f32_e32 v34, v82, v74
	v_min_f32_e32 v34, 0, v34
	v_mul_f32_e32 v34, 0x3fb8aa3b, v34
	v_exp_f32_e32 v34, v34
	v_sub_f32_e32 v54, v82, v75
	v_min_f32_e32 v54, 0, v54
	v_mfma_f32_16x16x32_bf16 v[50:53], v[50:53], v[66:69], v[58:61]
	v_mul_f32_e32 v76, v76, v34
	v_cndmask_b32_e32 v76, 0, v76, vcc
	v_cmp_gt_i32_e32 vcc, v32, v114
	v_mul_f32_e32 v34, v70, v34
	s_nop 0
	v_cndmask_b32_e64 v34, v34, 0, vcc
	v_cvt_pk_bf16_f32 v86, v76, v76
	v_mad_u64_u32 v[76:77], s[2:3], v114, s2, v[32:33]
	v_lshl_add_u32 v76, v76, 1, 0
	v_cvt_pk_bf16_f32 v34, v34, v34
	ds_write_b16 v76, v34 offset:36864
	v_sub_f32_e32 v34, v83, v74
	v_min_f32_e32 v34, 0, v34
	v_mul_f32_e32 v34, 0x3fb8aa3b, v34
	v_exp_f32_e32 v34, v34
	v_mul_f32_e32 v77, v79, v87
	v_or_b32_e32 v70, 1, v114
	ds_write_b16 v76, v86 offset:27648
	v_mul_f32_e32 v77, v77, v34
	v_cndmask_b32_e64 v77, v77, 0, vcc
	v_mul_f32_e32 v34, v71, v34
	v_cmp_le_i32_e32 vcc, v32, v70
	v_cvt_pk_bf16_f32 v77, v77, v77
	s_nop 0
	v_cndmask_b32_e32 v34, 0, v34, vcc
	v_cvt_pk_bf16_f32 v34, v34, v34
	ds_write_b16 v76, v34 offset:37008
	v_sub_f32_e32 v34, v84, v74
	v_min_f32_e32 v34, 0, v34
	v_mul_f32_e32 v34, 0x3fb8aa3b, v34
	v_exp_f32_e32 v34, v34
	ds_write_b16 v76, v77 offset:27792
	v_or_b32_e32 v71, 2, v114
	v_mul_f32_e32 v77, v80, v88
	v_cmp_lt_i32_e32 vcc, v32, v71
	v_mul_f32_e32 v77, v77, v34
	v_mul_f32_e32 v34, v72, v34
	v_cndmask_b32_e32 v77, 0, v77, vcc
	v_cmp_le_i32_e32 vcc, v32, v71
	v_mul_f32_e32 v54, 0x3fb8aa3b, v54
	v_exp_f32_e32 v54, v54
	v_cndmask_b32_e32 v34, 0, v34, vcc
	v_cvt_pk_bf16_f32 v34, v34, v34
	ds_write_b16 v76, v34 offset:37152
	v_sub_f32_e32 v34, v85, v74
	v_min_f32_e32 v34, 0, v34
	v_mul_f32_e32 v34, 0x3fb8aa3b, v34
	v_exp_f32_e32 v34, v34
	v_or_b32_e32 v72, 3, v114
	v_mul_f32_e32 v74, v81, v89
	v_cmp_lt_i32_e32 vcc, v32, v72
	v_mul_f32_e32 v74, v74, v34
	v_mul_f32_e32 v34, v73, v34
	v_cndmask_b32_e32 v74, 0, v74, vcc
	v_cmp_le_i32_e32 vcc, v32, v72
	v_mul_f32_e32 v50, v78, v50
	v_mul_f32_e32 v50, v50, v54
	v_cndmask_b32_e32 v34, 0, v34, vcc
	v_bfe_u32 v73, v34, 16, 1
	v_add3_u32 v34, v34, v73, s81
	ds_write_b16_d16_hi v76, v34 offset:37296
	v_or_b32_e32 v34, 16, v32
	v_cmp_lt_i32_e32 vcc, v34, v114
	v_mul_f32_e32 v46, v46, v54
	v_bfe_u32 v86, v77, 16, 1
	v_cndmask_b32_e32 v50, 0, v50, vcc
	v_cmp_gt_i32_e32 vcc, v34, v114
	v_cvt_pk_bf16_f32 v50, v50, v50
	ds_write_b16 v76, v50 offset:27680
	v_cndmask_b32_e64 v46, v46, 0, vcc
	v_cvt_pk_bf16_f32 v46, v46, v46
	ds_write_b16 v76, v46 offset:36896
	v_sub_f32_e32 v46, v83, v75
	v_min_f32_e32 v46, 0, v46
	v_mul_f32_e32 v46, 0x3fb8aa3b, v46
	v_exp_f32_e32 v46, v46
	v_mul_f32_e32 v50, v79, v51
	v_add3_u32 v77, v77, v86, s81
	ds_write_b16_d16_hi v76, v77 offset:27936
	v_mul_f32_e32 v50, v50, v46
	v_cndmask_b32_e64 v50, v50, 0, vcc
	v_mul_f32_e32 v46, v47, v46
	v_cmp_le_i32_e32 vcc, v34, v70
	v_cvt_pk_bf16_f32 v50, v50, v50
	s_nop 0
	v_cndmask_b32_e32 v46, 0, v46, vcc
	v_cvt_pk_bf16_f32 v46, v46, v46
	ds_write_b16 v76, v46 offset:37040
	v_sub_f32_e32 v46, v84, v75
	v_min_f32_e32 v46, 0, v46
	v_mul_f32_e32 v46, 0x3fb8aa3b, v46
	v_exp_f32_e32 v46, v46
	v_mul_f32_e32 v47, v80, v52
	v_cmp_lt_i32_e32 vcc, v34, v71
	ds_write_b16 v76, v50 offset:27824
	v_mul_f32_e32 v47, v47, v46
	v_cndmask_b32_e32 v47, 0, v47, vcc
	v_mul_f32_e32 v46, v48, v46
	v_cmp_le_i32_e32 vcc, v34, v71
	v_cvt_pk_bf16_f32 v47, v47, v47
	ds_write_b16 v76, v47 offset:27968
	v_cndmask_b32_e32 v46, 0, v46, vcc
	v_cvt_pk_bf16_f32 v46, v46, v46
	ds_write_b16 v76, v46 offset:37184
	v_sub_f32_e32 v46, v85, v75
	v_min_f32_e32 v46, 0, v46
	v_mul_f32_e32 v46, 0x3fb8aa3b, v46
	v_exp_f32_e32 v46, v46
	v_mul_f32_e32 v47, v81, v53
	v_cmp_lt_i32_e32 vcc, v34, v72
	v_bfe_u32 v77, v74, 16, 1
	v_mul_f32_e32 v47, v47, v46
	v_cndmask_b32_e32 v47, 0, v47, vcc
	v_mul_f32_e32 v46, v49, v46
	v_cmp_le_i32_e32 vcc, v34, v72
	v_cvt_pk_bf16_f32 v47, v47, v47
	ds_write_b16 v76, v47 offset:28112
	v_cndmask_b32_e32 v46, 0, v46, vcc
	v_add3_u32 v74, v74, v77, s81
	v_cvt_pk_bf16_f32 v46, v46, v46
	ds_write_b16_d16_hi v76, v74 offset:28080
	ds_write_b16 v76, v46 offset:37328
	v_mov_b32_e32 v33, s84
	ds_read_b128 v[46:49], v33 offset:57600
	ds_read_b128 v[50:53], v33 offset:57616
	s_waitcnt vmcnt(20)
; #define LAS __attribute__((address_space(3)))
; __device__ __forceinline__ unsigned f2bf(float f) { unsigned u = __float_as_uint(f); return (u + 0x7fffu + ((u >> 16) & 1u)) >> 16; }
; __device__ __forceinline__ void gdn_fetch(CArgs& a, int u, int w, int lane, GdnIn& in) {
;     const int chain = u / 36, n = u % 36, b = chain >> 3, h = (chain >> 1) & 3, dir = chain & 1;
;     const int r0 = scan_row(b, dir, n * 64), step = dir ? -1 : 1, fr = lane & 15, kg = lane >> 4;
; __device__ __forceinline__ float gdn_s1(const GdnIn& in, LAS unsigned char* ub, LAS unsigned char* dwb, int w, int lane) {
;     ...
;     { const f32x4 c8a = *(const LAS f32x4*)(GT + 64 + 8 * w), c8b = *(const LAS f32x4*)(GT + 64 + 8 * w + 4);
; #pragma unroll
;       for (int tt = 0; tt < 8; ++tt) KTT[lane * 72 + 8 * w + tt] = (bf16)f2bf(__uint_as_float(in.kt8[tt] << 16) * __expf(cl - (tt < 4 ? c8a[tt & 3] : c8b[tt & 3]))); }
;     asm volatile("s_waitcnt lgkmcnt(0)" ::: "memory");
	v_lshlrev_b32_e32 v55, 16, v137
	v_lshlrev_b32_e32 v54, 16, v135
	v_lshlrev_b32_e32 v57, 16, v133
	s_waitcnt lgkmcnt(1)
	v_sub_f32_e32 v46, s9, v46
	v_sub_f32_e32 v47, s9, v47
	v_sub_f32_e32 v48, s9, v48
	v_sub_f32_e32 v49, s9, v49
	v_mul_f32_e32 v46, 0x3fb8aa3b, v46
	v_mul_f32_e32 v47, 0x3fb8aa3b, v47
	v_mul_f32_e32 v48, 0x3fb8aa3b, v48
	v_mul_f32_e32 v49, 0x3fb8aa3b, v49
	v_exp_f32_e32 v46, v46
	v_exp_f32_e32 v47, v47
	v_exp_f32_e32 v48, v48
	v_exp_f32_e32 v49, v49
	s_waitcnt lgkmcnt(0)
	v_sub_f32_e32 v50, s9, v50
	v_sub_f32_e32 v51, s9, v51
	v_sub_f32_e32 v52, s9, v52
	v_sub_f32_e32 v53, s9, v53
	v_mul_f32_e32 v50, 0x3fb8aa3b, v50
	v_mul_f32_e32 v51, 0x3fb8aa3b, v51
	v_mul_f32_e32 v52, 0x3fb8aa3b, v52
	v_mul_f32_e32 v53, 0x3fb8aa3b, v53
	v_lshlrev_b32_e32 v56, 16, v131
	v_exp_f32_e32 v50, v50
	v_exp_f32_e32 v51, v51
	v_exp_f32_e32 v52, v52
	v_exp_f32_e32 v53, v53
	v_pk_mul_f32 v[46:47], v[46:47], v[56:57]
	v_pk_mul_f32 v[48:49], v[48:49], v[54:55]
	v_bfe_u32 v56, v47, 16, 1
	v_bfe_u32 v54, v49, 16, 1
	v_bfe_u32 v55, v48, 16, 1
	v_bfe_u32 v57, v46, 16, 1
	v_add3_u32 v57, v46, v57, s81
	v_add3_u32 v56, v47, v56, s81
	v_add3_u32 v55, v48, v55, s81
	v_add3_u32 v54, v49, v54, s81
	s_waitcnt vmcnt(16)
	v_lshlrev_b32_e32 v47, 16, v136
	v_lshlrev_b32_e32 v46, 16, v134
	v_lshlrev_b32_e32 v49, 16, v132
	v_lshlrev_b32_e32 v48, 16, v111
	v_pk_mul_f32 v[48:49], v[50:51], v[48:49]
	v_pk_mul_f32 v[46:47], v[52:53], v[46:47]
	v_bfe_u32 v52, v49, 16, 1
	v_bfe_u32 v50, v47, 16, 1
	v_bfe_u32 v51, v46, 16, 1
	v_bfe_u32 v53, v48, 16, 1
	v_mul_lo_u32 v33, v110, s75
	v_add3_u32 v48, v48, v53, s81
	v_add3_u32 v52, v49, v52, s81
	v_add3_u32 v46, v46, v51, s81
	v_add3_u32 v47, v47, v50, s81
	s_mov_b32 s2, 0x7060302
	v_add_u32_e32 v33, s11, v33
	v_perm_b32 v49, v47, v46, s2
	v_perm_b32 v48, v52, v48, s2
	v_perm_b32 v47, v54, v55, s2
	v_perm_b32 v46, v56, v57, s2
	ds_write_b128 v33, v[46:49] offset:46080
	s_waitcnt lgkmcnt(0)
	s_and_b64 vcc, exec, s[50:51]
	s_waitcnt lgkmcnt(0)
	s_barrier
	s_waitcnt vmcnt(0)
	v_lshlrev_b32_e32 v103, 16, v103
	v_lshlrev_b32_e32 v102, 16, v102
	v_lshlrev_b32_e32 v105, 16, v105
	v_lshlrev_b32_e32 v104, 16, v104
	v_lshlrev_b32_e32 v99, 16, v99
	v_lshlrev_b32_e32 v98, 16, v98
	v_lshlrev_b32_e32 v101, 16, v101
	v_lshlrev_b32_e32 v100, 16, v100
	v_lshlrev_b32_e32 v96, 16, v96
	v_lshlrev_b32_e32 v94, 16, v94
	v_lshlrev_b32_e32 v97, 16, v97
	v_lshlrev_b32_e32 v95, 16, v95
	v_lshlrev_b32_e32 v92, 16, v92
	v_lshlrev_b32_e32 v90, 16, v90
	v_lshlrev_b32_e32 v93, 16, v93
	v_lshlrev_b32_e32 v91, 16, v91
	s_cbranch_vccnz .LBB0_1781
	s_add_i32 s2, s26, 2
	s_mul_hi_i32 s3, s2, 0x38e38e39
	s_lshr_b32 s20, s3, 31
	s_ashr_i32 s3, s3, 3
	s_add_i32 s3, s3, s20
	s_mul_i32 s20, s3, 36
	s_sub_i32 s2, s2, s20
	s_ashr_i32 s36, s3, 3
	s_and_b32 s20, s3, 1
	s_lshl_b32 s29, s2, 6
	s_cmp_gt_i32 s2, 3
	s_mov_b64 s[26:27], -1
	s_cbranch_scc0 .LBB0_1778
	s_add_i32 s2, s29, 0xffffff00
	s_lshl_b32 s26, s36, 11
	s_sub_i32 s27, 0x8ff, s29
	s_cmp_eq_u32 s20, 0
	s_cselect_b32 s2, s2, s27
	s_add_i32 s2, s26, s2
	s_addk_i32 s2, 0x1000
	s_mov_b64 s[26:27], 0
